# speedup vs baseline: 1.0112x; 1.0080x over previous
.LBB2_4:
	s_and_b32 s0, s23, 0x3fffffc0
	s_lshl_b32 s0, s0, 2
	s_lshl_b64 s[10:11], s[2:3], 9
	s_add_i32 s23, s0, 0
	s_add_u32 s0, s14, 0x6000
	s_waitcnt vmcnt(0) lgkmcnt(0)
	s_barrier
	s_addc_u32 s1, s15, 0
	s_mov_b32 s2, m0
	s_mov_b32 m0, s24
	s_nop 0
	global_load_lds_dwordx4 v189, s[0:1]
	s_mov_b32 m0, s2
	s_add_u32 s0, s12, 0x2000
	s_addc_u32 s1, s13, 0
	s_cmp_lg_u32 0, -1
	s_cselect_b32 s2, 0, 0
	s_add_i32 s2, s2, s22
	s_add_i32 s2, s2, 0x8000
	s_mov_b32 s4, m0
	s_mov_b32 m0, s2
	s_nop 0
	global_load_lds_dwordx4 v189, s[0:1]
	s_mov_b32 m0, s4
	ds_read_b128 v[172:175], v190 offset:8192
	ds_read_b128 v[168:171], v190 offset:8704
	ds_read_b128 v[164:167], v190 offset:10240
	ds_read_b128 v[160:163], v190 offset:10752
	ds_read_b128 v[156:159], v190 offset:12288
	ds_read_b128 v[152:155], v190 offset:12800
	ds_read_b128 v[148:151], v190 offset:14336
	ds_read_b128 v[144:147], v190 offset:14848
	s_mov_b32 s3, 0
	s_add_i32 s2, s28, s27
	s_lshl_b64 s[4:5], s[2:3], 18
	v_lshlrev_b32_e32 v2, 1, v1
	v_lshlrev_b32_e32 v3, 3, v0
	s_add_u32 s2, s8, s4
	v_and_b32_e32 v2, 32, v2
	v_and_b32_e32 v3, 24, v3
	v_lshlrev_b32_e32 v185, 4, v0
	s_waitcnt vmcnt(2) lgkmcnt(0)
	s_barrier
	s_addc_u32 s4, s9, s5
	v_add3_u32 v2, 0, v2, v3
	v_lshlrev_b32_e32 v3, 8, v18
	v_and_b32_e32 v0, 0xc0, v185
	s_add_u32 s27, s2, 0x2000
	v_mov_b32_e32 v188, 0
	v_mov_b32_e32 v192, 0
	v_lshrrev_b32_e32 v183, 4, v1
	v_add3_u32 v187, v2, v3, v0
	s_mov_b32 s26, -1
	v_cmp_gt_u32_e64 s[0:1], 32, v1
	v_lshl_add_u32 v186, v181, 2, s23
	s_addc_u32 s28, s4, 0
	s_movk_i32 s29, 0x4000
	s_movk_i32 s31, 0x2000
	s_mov_b64 s[8:9], 0
	s_mov_b32 s30, 0x41000000
	v_mov_b32_e32 v0, 0
	v_mov_b32_e32 v1, v188
	v_mov_b32_e32 v2, v188
	v_mov_b32_e32 v3, v188
	v_mov_b32_e32 v4, v188
	v_mov_b32_e32 v5, v188
	v_mov_b32_e32 v6, v188
	v_mov_b32_e32 v7, v188
	v_mov_b32_e32 v8, v188
	v_mov_b32_e32 v9, v188
	v_mov_b32_e32 v10, v188
	v_mov_b32_e32 v11, v188
	v_mov_b32_e32 v12, v188
	v_mov_b32_e32 v13, v188
	v_mov_b32_e32 v14, v188
	v_mov_b32_e32 v15, v188
	v_mov_b32_e32 v16, 0
	v_mov_b32_e32 v17, v188
	v_mov_b32_e32 v18, v188
	v_mov_b32_e32 v19, v188
	v_mov_b32_e32 v20, v188
	v_mov_b32_e32 v21, v188
	v_mov_b32_e32 v22, v188
	v_mov_b32_e32 v23, v188
	v_mov_b32_e32 v24, v188
	v_mov_b32_e32 v25, v188
	v_mov_b32_e32 v26, v188
	v_mov_b32_e32 v27, v188
	v_mov_b32_e32 v28, v188
	v_mov_b32_e32 v29, v188
	v_mov_b32_e32 v30, v188
	v_mov_b32_e32 v31, v188
	s_cmp_ge_u32 s20, 4
	s_cbranch_scc0 .Lattn_prio_done
	s_setprio 1
.Lattn_prio_done:
.LBB2_5:
	s_add_i32 s26, s26, 2
	v_add_u32_e32 v191, s3, v187
	ds_read_b64_tr_b16 v[176:177], v191 offset:24576
	ds_read_b64_tr_b16 v[178:179], v191 offset:25088
	v_mfma_f32_32x32x16_f16 v[96:111], v[172:175], v[124:127], v[32:47]
	v_exp_f32_e32 v56, v56
	v_exp_f32_e32 v57, v57
	v_cvt_pk_f16_f32 v140, v64, v65
	v_cvt_pk_f16_f32 v141, v66, v67
	ds_read_b64_tr_b16 v[172:173], v191 offset:28672
	ds_read_b64_tr_b16 v[174:175], v191 offset:29184
	v_mfma_f32_32x32x16_f16 v[80:95], v[168:171], v[124:127], v[32:47]
	v_exp_f32_e32 v58, v58
	v_exp_f32_e32 v59, v59
	v_pk_add_f16 v128, v140, v141
	v_cvt_pk_f16_f32 v142, v68, v69
	v_cvt_pk_f16_f32 v143, v70, v71
	ds_read_b64_tr_b16 v[64:65], v191 offset:25600
	ds_read_b64_tr_b16 v[66:67], v191 offset:26112
	v_mfma_f32_32x32x16_f16 v[96:111], v[164:167], v[120:123], v[96:111]
	v_exp_f32_e32 v60, v60
	v_exp_f32_e32 v61, v61
	v_pk_add_f16 v129, v142, v143
	v_cvt_pk_f16_f32 v136, v72, v73
	v_cvt_pk_f16_f32 v137, v74, v75
	ds_read_b64_tr_b16 v[68:69], v191 offset:29696
	ds_read_b64_tr_b16 v[70:71], v191 offset:30208
	v_mfma_f32_32x32x16_f16 v[80:95], v[160:163], v[120:123], v[80:95]
	v_exp_f32_e32 v62, v62
	v_exp_f32_e32 v63, v63
	v_pk_add_f16 v72, v136, v137
	v_pk_add_f16 v128, v128, v129
	v_cvt_pk_f16_f32 v138, v76, v77
	v_cvt_pk_f16_f32 v139, v78, v79
	s_min_u32 s2, s26, 28
	s_lshl_b32 s2, s2, 13
	s_add_u32 s2, s14, s2
	s_addc_u32 s3, s15, 0
	s_add_u32 s2, s2, 0x6000
	s_addc_u32 s3, s3, 0
	s_add_i32 s4, s31, s24
	s_mov_b32 s5, m0
	s_mov_b32 m0, s4
	s_nop 0
	global_load_lds_dwordx4 v189, s[2:3]
	s_mov_b32 m0, s5
	ds_read_b64_tr_b16 v[76:77], v191 offset:26624
	ds_read_b64_tr_b16 v[78:79], v191 offset:27136
	v_mfma_f32_32x32x16_f16 v[96:111], v[156:159], v[116:119], v[96:111]
	v_pk_add_f16 v73, v138, v139
	v_cvt_pk_f16_f32 v132, v48, v49
	v_cvt_pk_f16_f32 v133, v50, v51
	ds_read_b64_tr_b16 v[48:49], v191 offset:30720
	ds_read_b64_tr_b16 v[50:51], v191 offset:31232
	v_mfma_f32_32x32x16_f16 v[80:95], v[152:155], v[116:119], v[80:95]
	v_pk_add_f16 v129, v72, v73
	v_cvt_pk_f16_f32 v134, v52, v53
	v_cvt_pk_f16_f32 v135, v54, v55
	v_pk_add_f16 v156, v132, v133
	s_add_u32 s2, s27, 0x2000
	s_addc_u32 s3, s28, 0
	s_add_i32 s4, s29, s25
	s_mov_b32 s5, m0
	s_mov_b32 m0, s4
	s_nop 0
	global_load_lds_dwordx4 v189, s[2:3]
	s_mov_b32 m0, s5
	ds_read_b64_tr_b16 v[72:73], v191 offset:27648
	ds_read_b64_tr_b16 v[74:75], v191 offset:28160
	v_mfma_f32_32x32x16_f16 v[96:111], v[148:151], v[112:115], v[96:111]
	v_pk_add_f16 v153, v128, v129
	v_cvt_pk_f16_f32 v128, v56, v57
	v_cvt_pk_f16_f32 v129, v58, v59
	v_pk_add_f16 v152, v134, v135
	ds_read_b64_tr_b16 v[52:53], v191 offset:31744
	ds_read_b64_tr_b16 v[54:55], v191 offset:32256
	v_mfma_f32_32x32x16_f16 v[80:95], v[144:147], v[112:115], v[80:95]
	v_pk_add_f16 v56, v128, v129
	v_pk_add_f16 v57, v156, v152
	v_cvt_pk_f16_f32 v130, v60, v61
	v_cvt_pk_f16_f32 v131, v62, v63
	s_andn2_b64 vcc, exec, s[18:19]
	v_pk_add_f16 v57, v153, v57
	v_pk_add_f16 v58, v130, v131
	s_cbranch_vccnz .LBB2_7
	v_pk_add_f16 v59, v56, v58
	v_max3_f32 v61, v96, v97, v80
	v_max3_f32 v62, v98, v99, v81
	s_mov_b64 s[8:9], 0
	v_pk_add_f16 v59, v57, v59
	s_nop 0
	v_cvt_f32_f16_e32 v60, v59
	v_cvt_f32_f16_sdwa v59, v59 dst_sel:DWORD dst_unused:UNUSED_PAD src0_sel:WORD_1
	v_add_f32_e32 v59, v59, v60
	v_add_f32_e32 v188, v188, v59
	v_max3_f32 v59, v61, v82, v83
	v_max3_f32 v60, v62, v102, v103
	s_nop 0
	v_max3_f32 v59, v59, v100, v101
	v_max3_f32 v60, v60, v86, v87
	s_nop 0
	v_max3_f32 v59, v59, v84, v85
	v_max3_f32 v60, v60, v106, v107
	s_nop 0
	v_max3_f32 v59, v59, v104, v105
	v_max3_f32 v60, v60, v90, v91
	s_nop 0
	v_max3_f32 v59, v59, v88, v89
	v_max3_f32 v60, v60, v110, v111
	s_nop 0
	v_max3_f32 v59, v59, v108, v109
	v_max3_f32 v60, v60, v94, v95
	s_nop 0
	v_max3_f32 v59, v59, v92, v93
	s_nop 0
	v_max_f32 v59, v59, v60
	s_nop 0
	v_mov_b32_e32 v60, v59
	s_nop 1
	v_permlane32_swap_b32_e32 v59, v60
	v_max_f32 v59, v59, v60
	s_nop 0
	v_cmp_lt_f32_e32 vcc, s30, v59
	s_cbranch_vccnz .LBB2_19
.LBB2_7:
	s_waitcnt lgkmcnt(14)
	v_mfma_f32_32x32x16_f16 v[0:15], v[140:143], v[176:179], v[0:15]
	v_pk_add_f16 v56, v56, v58
	v_exp_f32_e32 v96, v96
	v_pk_add_f16 v56, v57, v56
	v_exp_f32_e32 v97, v97
	v_exp_f32_e32 v98, v98
	s_andn2_b64 vcc, exec, s[16:17]
	s_cbranch_vccnz .LBB2_9
	v_fma_mix_f32 v188, v56, 1.0, v188 op_sel_hi:[1,0,0]
	v_fma_mix_f32 v192, v56, 1.0, v192 op_sel:[1,0,0] op_sel_hi:[1,0,0]

.LBB2_11:
	s_add_i32 s33, s29, 0x2000
	s_cmpk_lg_i32 s29, 0x4000
	s_cselect_b32 s33, s33, 0
	v_add_u32_e32 v191, s31, v187
	ds_read_b64_tr_b16 v[148:149], v191 offset:24576
	ds_read_b64_tr_b16 v[150:151], v191 offset:25088
	s_waitcnt lgkmcnt(9)
	v_mfma_f32_32x32x16_f16 v[64:79], v[56:59], v[124:127], v[32:47]
	v_exp_f32_e32 v88, v88
	v_exp_f32_e32 v89, v89
	v_cvt_pk_f16_f32 v140, v96, v97
	v_cvt_pk_f16_f32 v141, v98, v99
	ds_read_b64_tr_b16 v[144:145], v191 offset:28672
	ds_read_b64_tr_b16 v[146:147], v191 offset:29184
	s_waitcnt lgkmcnt(10)
	v_mfma_f32_32x32x16_f16 v[48:63], v[176:179], v[124:127], v[32:47]
	v_exp_f32_e32 v90, v90
	v_exp_f32_e32 v91, v91
	v_pk_add_f16 v128, v140, v141
	v_cvt_pk_f16_f32 v142, v100, v101
	v_cvt_pk_f16_f32 v143, v102, v103
	ds_read_b64_tr_b16 v[96:97], v191 offset:25600
	ds_read_b64_tr_b16 v[98:99], v191 offset:26112
	s_waitcnt lgkmcnt(11)
	v_mfma_f32_32x32x16_f16 v[64:79], v[172:175], v[120:123], v[64:79]
	v_exp_f32_e32 v92, v92
	v_exp_f32_e32 v93, v93
	v_pk_add_f16 v129, v142, v143
	v_cvt_pk_f16_f32 v136, v104, v105
	v_cvt_pk_f16_f32 v137, v106, v107
	ds_read_b64_tr_b16 v[100:101], v191 offset:29696
	ds_read_b64_tr_b16 v[102:103], v191 offset:30208
	s_waitcnt lgkmcnt(12)
	v_mfma_f32_32x32x16_f16 v[48:63], v[168:171], v[120:123], v[48:63]
	v_exp_f32_e32 v94, v94
	v_exp_f32_e32 v95, v95
	v_pk_add_f16 v128, v128, v129
	v_cvt_pk_f16_f32 v138, v108, v109
	v_cvt_pk_f16_f32 v139, v110, v111
	v_pk_add_f16 v172, v136, v137
	s_min_u32 s31, s26, 27
	s_lshl_b32 s31, s31, 13
	s_add_u32 s31, s14, s31
	s_addc_u32 s35, s15, 0
	s_add_u32 s34, s31, 0x8000
	s_addc_u32 s35, s35, 0
	s_add_i32 s31, s29, s24
	s_mov_b32 s36, m0
	s_mov_b32 m0, s31
	s_nop 0
	global_load_lds_dwordx4 v189, s[34:35]
	s_mov_b32 m0, s36
	ds_read_b64_tr_b16 v[104:105], v191 offset:26624
	ds_read_b64_tr_b16 v[106:107], v191 offset:27136
	s_waitcnt lgkmcnt(13)
	v_mfma_f32_32x32x16_f16 v[64:79], v[164:167], v[116:119], v[64:79]
	v_pk_add_f16 v108, v138, v139
	v_cvt_pk_f16_f32 v132, v80, v81
	v_cvt_pk_f16_f32 v133, v82, v83
	ds_read_b64_tr_b16 v[80:81], v191 offset:30720
	ds_read_b64_tr_b16 v[82:83], v191 offset:31232
	s_waitcnt lgkmcnt(14)
	v_mfma_f32_32x32x16_f16 v[48:63], v[160:163], v[116:119], v[48:63]
	v_pk_add_f16 v129, v172, v108
	v_cvt_pk_f16_f32 v134, v84, v85
	v_cvt_pk_f16_f32 v135, v86, v87
	v_pk_add_f16 v164, v132, v133
	s_add_u32 s34, s27, 0x4000
	s_addc_u32 s35, s28, 0
	s_add_i32 s31, s33, s25
	s_mov_b32 s36, m0
	s_mov_b32 m0, s31
	s_nop 0
	global_load_lds_dwordx4 v189, s[34:35]
	s_mov_b32 m0, s36
	ds_read_b64_tr_b16 v[108:109], v191 offset:27648
	ds_read_b64_tr_b16 v[110:111], v191 offset:28160
	s_waitcnt lgkmcnt(14)
	v_mfma_f32_32x32x16_f16 v[64:79], v[156:159], v[112:115], v[64:79]
	v_pk_add_f16 v161, v128, v129
	v_cvt_pk_f16_f32 v128, v88, v89
	v_cvt_pk_f16_f32 v129, v90, v91
	v_pk_add_f16 v160, v134, v135
	ds_read_b64_tr_b16 v[84:85], v191 offset:31744
	ds_read_b64_tr_b16 v[86:87], v191 offset:32256
	v_mfma_f32_32x32x16_f16 v[48:63], v[152:155], v[112:115], v[48:63]
	v_pk_add_f16 v88, v128, v129
	v_pk_add_f16 v89, v164, v160
	v_cvt_pk_f16_f32 v130, v92, v93
	v_cvt_pk_f16_f32 v131, v94, v95
	s_and_b64 vcc, exec, s[16:17]
	v_pk_add_f16 v89, v161, v89
	v_pk_add_f16 v90, v130, v131
	s_cbranch_vccnz .LBB2_13
	v_pk_add_f16 v91, v88, v90
	v_max3_f32 v93, v64, v65, v48
	v_max3_f32 v94, v66, v67, v49
	s_mov_b64 s[8:9], 0
	v_pk_add_f16 v91, v89, v91
	s_nop 0
	v_cvt_f32_f16_e32 v92, v91
	v_cvt_f32_f16_sdwa v91, v91 dst_sel:DWORD dst_unused:UNUSED_PAD src0_sel:WORD_1
	v_add_f32_e32 v91, v91, v92
	v_add_f32_e32 v188, v188, v91
	v_max3_f32 v91, v93, v50, v51
	v_max3_f32 v92, v94, v70, v71
	s_nop 0
	v_max3_f32 v91, v91, v68, v69
	v_max3_f32 v92, v92, v54, v55
	s_nop 0
	v_max3_f32 v91, v91, v52, v53
	v_max3_f32 v92, v92, v74, v75
	s_nop 0
	v_max3_f32 v91, v91, v72, v73
	v_max3_f32 v92, v92, v58, v59
	s_nop 0
	v_max3_f32 v91, v91, v56, v57
	v_max3_f32 v92, v92, v78, v79
	s_nop 0
	v_max3_f32 v91, v91, v76, v77
	v_max3_f32 v92, v92, v62, v63
	s_nop 0
	v_max3_f32 v91, v91, v60, v61
	s_nop 0
	v_max_f32 v91, v91, v92
	s_nop 0
	v_mov_b32_e32 v92, v91
	s_nop 1
	v_permlane32_swap_b32_e32 v91, v92
	v_max_f32 v91, v91, v92
	s_nop 0
	v_cmp_lt_f32_e32 vcc, s30, v91
	s_cbranch_vccnz .LBB2_22
.LBB2_13:
	s_waitcnt lgkmcnt(14)
	v_mfma_f32_32x32x16_f16 v[0:15], v[140:143], v[148:151], v[0:15]
	v_pk_add_f16 v88, v88, v90
	v_exp_f32_e32 v64, v64
	v_pk_add_f16 v88, v89, v88
	v_exp_f32_e32 v65, v65
	v_exp_f32_e32 v66, v66
	s_and_b64 vcc, exec, s[18:19]
	s_cbranch_vccnz .LBB2_15
	v_fma_mix_f32 v188, v88, 1.0, v188 op_sel_hi:[1,0,0]
	v_fma_mix_f32 v192, v88, 1.0, v192 op_sel:[1,0,0] op_sel_hi:[1,0,0]

.Lattn_exit_fix:
	s_mov_b64 s[2:3], s[16:17]
	s_mov_b64 s[4:5], s[18:19]
	s_branch .LBB2_25

.LBB2_31:
	v_add_f32_e32 v188, v188, v192
	v_exp_f32_e32 v49, v40
	v_add_f32_e32 v40, v80, v81
	v_add_f32_e32 v40, v40, v82
	v_add_f32_e32 v40, v40, v83
	v_add_f32_e32 v40, v40, v84
	v_exp_f32_e32 v62, v41
	v_exp_f32_e32 v63, v42
	v_exp_f32_e32 v64, v43
	v_exp_f32_e32 v65, v44
	v_exp_f32_e32 v66, v45
	v_exp_f32_e32 v67, v46
	v_exp_f32_e32 v68, v47
	v_add_f32_e32 v50, v40, v85
	v_cvt_pk_f16_f32 v40, v80, v81
	v_cvt_pk_f16_f32 v41, v82, v83
	v_cvt_pk_f16_f32 v42, v84, v85
	v_cvt_pk_f16_f32 v43, v86, v87
	ds_read_b64_tr_b16 v[44:45], v187 offset:32768
	ds_read_b64_tr_b16 v[46:47], v187 offset:33280
	v_add_f32_e32 v50, v50, v86
	v_add_f32_e32 v54, v50, v87
	ds_read_b64_tr_b16 v[50:51], v187 offset:33792
	ds_read_b64_tr_b16 v[52:53], v187 offset:34304
	s_waitcnt lgkmcnt(2)
	v_mfma_f32_32x32x16_f16 v[0:15], v[40:43], v[44:47], v[0:15]
	ds_read_b64_tr_b16 v[44:45], v187 offset:36864
	ds_read_b64_tr_b16 v[46:47], v187 offset:37376
	v_add_f32_e32 v54, v54, v88
	v_add_f32_e32 v69, v54, v89
	v_cvt_pk_f16_f32 v54, v88, v89
	v_cvt_pk_f16_f32 v55, v90, v91
	v_cvt_pk_f16_f32 v56, v92, v93
	v_cvt_pk_f16_f32 v57, v94, v95
	s_waitcnt lgkmcnt(0)
	v_mfma_f32_32x32x16_f16 v[16:31], v[40:43], v[44:47], v[16:31]
	v_add_f32_e32 v40, v69, v90
	v_add_f32_e32 v40, v40, v91
	v_add_f32_e32 v40, v40, v92
	v_add_f32_e32 v40, v40, v93
	ds_read_b64_tr_b16 v[58:59], v187 offset:37888
	ds_read_b64_tr_b16 v[60:61], v187 offset:38400
	v_add_f32_e32 v40, v40, v94
	v_add_f32_e32 v40, v40, v95
	v_mfma_f32_32x32x16_f16 v[0:15], v[54:57], v[50:53], v[0:15]
	v_add_f32_e32 v40, v40, v32
	v_add_f32_e32 v50, v40, v33
	v_cvt_pk_f16_f32 v40, v32, v33
	v_cvt_pk_f16_f32 v41, v34, v35
	v_cvt_pk_f16_f32 v42, v36, v37
	v_cvt_pk_f16_f32 v43, v38, v39
	ds_read_b64_tr_b16 v[44:45], v187 offset:34816
	ds_read_b64_tr_b16 v[46:47], v187 offset:35328
	s_waitcnt lgkmcnt(2)
	v_mfma_f32_32x32x16_f16 v[16:31], v[54:57], v[58:61], v[16:31]
	v_add_f32_e32 v32, v50, v34
	v_add_f32_e32 v50, v32, v35
	ds_read_b64_tr_b16 v[32:33], v187 offset:35840
	ds_read_b64_tr_b16 v[34:35], v187 offset:36352
	v_add_f32_e32 v36, v50, v36
	v_add_f32_e32 v36, v36, v37
	v_cvt_pk_f16_f32 v50, v49, v62
	v_cvt_pk_f16_f32 v51, v63, v64
	s_waitcnt lgkmcnt(2)
	v_mfma_f32_32x32x16_f16 v[0:15], v[40:43], v[44:47], v[0:15]
	ds_read_b64_tr_b16 v[44:45], v187 offset:38912
	ds_read_b64_tr_b16 v[46:47], v187 offset:39424
	v_cvt_pk_f16_f32 v52, v65, v66
	v_cvt_pk_f16_f32 v53, v67, v68
	ds_read_b64_tr_b16 v[54:55], v187 offset:39936
	ds_read_b64_tr_b16 v[56:57], v187 offset:40448
	v_add_f32_e32 v36, v36, v38
	v_add_f32_e32 v36, v36, v39
	v_add_f32_e32 v36, v36, v49
	s_waitcnt lgkmcnt(2)
	v_mfma_f32_32x32x16_f16 v[16:31], v[40:43], v[44:47], v[16:31]
	v_add_f32_e32 v36, v36, v62
	v_mfma_f32_32x32x16_f16 v[0:15], v[50:53], v[32:35], v[0:15]
	v_add_f32_e32 v32, v36, v63
	v_add_f32_e32 v32, v32, v64
	v_add_f32_e32 v32, v32, v65
	v_add_f32_e32 v32, v32, v66
	v_add_f32_e32 v32, v32, v67
	v_add_f32_e32 v32, v32, v68
	v_add_f32_e32 v32, v188, v32
	s_waitcnt lgkmcnt(0)
	v_mfma_f32_32x32x16_f16 v[16:31], v[50:53], v[54:57], v[16:31]
	v_mov_b32_e32 v33, v32
	s_nop 1
	v_permlane32_swap_b32_e32 v32, v33
	s_and_saveexec_b64 s[2:3], s[0:1]
	v_add_f32_e32 v32, v32, v33
	ds_write_b32 v186, v32 offset:49280
	s_or_b64 exec, exec, s[2:3]
	s_waitcnt lgkmcnt(0)
	ds_read_b128 v[32:35], v48 offset:49280
	ds_read_b128 v[36:39], v48 offset:49312
	s_lshl_b64 s[0:1], s[10:11], 2
	s_add_u32 s0, s6, s0
	s_addc_u32 s1, s7, s1
	s_waitcnt lgkmcnt(1)
	v_rcp_f32_e32 v40, v32
	v_rcp_f32_e32 v41, v33
	s_lshl_b32 s2, s20, 13
	v_rcp_f32_e32 v42, v34
	v_rcp_f32_e32 v43, v35
	s_waitcnt lgkmcnt(0)
	v_rcp_f32_e32 v44, v36
	ds_read_b128 v[32:35], v48 offset:49344
	v_rcp_f32_e32 v45, v37
	v_rcp_f32_e32 v46, v38
	v_rcp_f32_e32 v47, v39
	ds_read_b128 v[36:39], v48 offset:49376
	s_add_i32 s2, s2, 0
	v_lshlrev_b32_e32 v48, 2, v181
	v_add3_u32 v48, s2, v182, v48
	v_mul_f32_e32 v0, v0, v40
	v_mul_f32_e32 v16, v16, v40
	v_add_u32_e32 v40, 0xc800, v48
	ds_write2_b32 v40, v0, v16 offset1:32
	v_mul_f32_e32 v0, v1, v41
	v_mul_f32_e32 v1, v17, v41
	ds_write2_b32 v40, v0, v1 offset0:64 offset1:96
	v_mul_f32_e32 v0, v2, v42
	v_mul_f32_e32 v1, v18, v42
	ds_write2_b32 v40, v0, v1 offset0:128 offset1:160
	v_mul_f32_e32 v0, v3, v43
	v_mul_f32_e32 v1, v19, v43
	s_waitcnt lgkmcnt(4)
	v_rcp_f32_e32 v32, v32
	ds_write2_b32 v40, v0, v1 offset0:192 offset1:224
	v_mul_f32_e32 v0, v4, v44
	v_mul_f32_e32 v1, v20, v44
	v_add_u32_e32 v2, 0xd000, v48
	v_rcp_f32_e32 v33, v33
	ds_write2_b32 v2, v0, v1 offset1:32
	v_mul_f32_e32 v0, v5, v45
	v_mul_f32_e32 v1, v21, v45
	v_rcp_f32_e32 v34, v34
	ds_write2_b32 v2, v0, v1 offset0:64 offset1:96
	v_mul_f32_e32 v0, v6, v46
	v_mul_f32_e32 v1, v22, v46
	v_rcp_f32_e32 v35, v35
	ds_write2_b32 v2, v0, v1 offset0:128 offset1:160
	v_mul_f32_e32 v0, v7, v47
	v_mul_f32_e32 v1, v23, v47
	s_waitcnt lgkmcnt(7)
	v_rcp_f32_e32 v36, v36
	ds_write2_b32 v2, v0, v1 offset0:192 offset1:224
	v_mul_f32_e32 v0, v8, v32
	v_mul_f32_e32 v1, v24, v32
	v_add_u32_e32 v2, 0xd800, v48
	v_rcp_f32_e32 v37, v37
	ds_write2_b32 v2, v0, v1 offset1:32
	v_mul_f32_e32 v0, v9, v33
	v_mul_f32_e32 v1, v25, v33
	v_rcp_f32_e32 v38, v38
	ds_write2_b32 v2, v0, v1 offset0:64 offset1:96
	v_mul_f32_e32 v0, v10, v34
	v_mul_f32_e32 v1, v26, v34
	v_rcp_f32_e32 v39, v39
	ds_write2_b32 v2, v0, v1 offset0:128 offset1:160
	v_mul_f32_e32 v0, v11, v35
	v_mul_f32_e32 v1, v27, v35
	ds_write2_b32 v2, v0, v1 offset0:192 offset1:224
	v_mul_f32_e32 v0, v12, v36
	v_mul_f32_e32 v1, v28, v36
	v_add_u32_e32 v2, 0xe000, v48
	ds_write2_b32 v2, v0, v1 offset1:32
	v_mul_f32_e32 v0, v13, v37
	v_mul_f32_e32 v1, v29, v37
	ds_write2_b32 v2, v0, v1 offset0:64 offset1:96
	v_mul_f32_e32 v0, v14, v38
	v_mul_f32_e32 v1, v30, v38
	ds_write2_b32 v2, v0, v1 offset0:128 offset1:160
	v_mul_f32_e32 v0, v15, v39
	v_mul_f32_e32 v1, v31, v39
	v_and_b32_e32 v8, 0xf0, v185
	ds_write2_b32 v2, v0, v1 offset0:192 offset1:224
	v_add_u32_e32 v14, s2, v8
	s_waitcnt lgkmcnt(0)
	v_lshl_add_u32 v0, v183, 8, v14
	v_or_b32_e32 v15, 4, v183
	s_lshl_b32 s3, s21, 2
	ds_read_b128 v[0:3], v0 offset:51200
	v_lshl_add_u32 v4, v15, 8, v14
	s_add_u32 s0, s0, s3
	ds_read_b128 v[4:7], v4 offset:51200
	s_addc_u32 s1, s1, 0
	v_mov_b32_e32 v9, 0
	v_lshl_add_u64 v[10:11], s[0:1], 0, v[8:9]
	v_lshlrev_b32_e32 v8, 11, v183
	v_lshl_add_u64 v[12:13], v[10:11], 0, v[8:9]
	v_lshlrev_b32_e32 v8, 11, v15
	s_waitcnt lgkmcnt(1)
	global_store_dwordx4 v[12:13], v[0:3], off sc1
	v_or_b32_e32 v15, 12, v183
	s_nop 0
	v_lshl_add_u64 v[0:1], v[10:11], 0, v[8:9]
	s_waitcnt lgkmcnt(0)
	global_store_dwordx4 v[0:1], v[4:7], off sc1
	s_nop 1
	v_or_b32_e32 v4, 8, v183
	v_lshl_add_u32 v0, v4, 8, v14
	ds_read_b128 v[0:3], v0 offset:51200
	v_lshlrev_b32_e32 v8, 11, v4
	v_lshl_add_u32 v4, v15, 8, v14
	ds_read_b128 v[4:7], v4 offset:51200
	v_lshl_add_u64 v[12:13], v[10:11], 0, v[8:9]
	v_lshlrev_b32_e32 v8, 11, v15
	s_waitcnt lgkmcnt(1)
	global_store_dwordx4 v[12:13], v[0:3], off sc1
	v_or_b32_e32 v15, 20, v183
	s_nop 0
	v_lshl_add_u64 v[0:1], v[10:11], 0, v[8:9]
	s_waitcnt lgkmcnt(0)
	global_store_dwordx4 v[0:1], v[4:7], off sc1
	s_nop 1
	v_or_b32_e32 v4, 16, v183
	v_lshl_add_u32 v0, v4, 8, v14
	ds_read_b128 v[0:3], v0 offset:51200
	v_lshlrev_b32_e32 v8, 11, v4
	v_lshl_add_u32 v4, v15, 8, v14
	ds_read_b128 v[4:7], v4 offset:51200
	v_lshl_add_u64 v[12:13], v[10:11], 0, v[8:9]
	v_lshlrev_b32_e32 v8, 11, v15
	s_waitcnt lgkmcnt(1)
	global_store_dwordx4 v[12:13], v[0:3], off sc1
	v_or_b32_e32 v15, 28, v183
	s_nop 0
	v_lshl_add_u64 v[0:1], v[10:11], 0, v[8:9]
	s_waitcnt lgkmcnt(0)
	global_store_dwordx4 v[0:1], v[4:7], off sc1
	s_nop 1
	v_or_b32_e32 v4, 24, v183
	v_lshl_add_u32 v0, v4, 8, v14
	ds_read_b128 v[0:3], v0 offset:51200
	v_lshlrev_b32_e32 v8, 11, v4
	v_lshl_add_u32 v4, v15, 8, v14
	ds_read_b128 v[4:7], v4 offset:51200
	v_lshl_add_u64 v[12:13], v[10:11], 0, v[8:9]
	v_lshlrev_b32_e32 v8, 11, v15
	s_waitcnt lgkmcnt(1)
	global_store_dwordx4 v[12:13], v[0:3], off sc1
	s_nop 1
	v_lshl_add_u64 v[0:1], v[10:11], 0, v[8:9]
	s_waitcnt lgkmcnt(0)
	global_store_dwordx4 v[0:1], v[4:7], off sc1
	s_endpgm

	.amdhsa_kernel _Z11attn_kernelPKDF16_S0_S0_PKjPf
		.amdhsa_group_segment_fixed_size 0
		.amdhsa_private_segment_fixed_size 0
		.amdhsa_kernarg_size 40
		.amdhsa_user_sgpr_count 2
		.amdhsa_user_sgpr_dispatch_ptr 0
		.amdhsa_user_sgpr_queue_ptr 0
		.amdhsa_user_sgpr_kernarg_segment_ptr 1
		.amdhsa_user_sgpr_dispatch_id 0
		.amdhsa_user_sgpr_kernarg_preload_length 0
		.amdhsa_user_sgpr_kernarg_preload_offset 0
		.amdhsa_user_sgpr_private_segment_size 0
		.amdhsa_uses_dynamic_stack 0
		.amdhsa_enable_private_segment 0
		.amdhsa_system_sgpr_workgroup_id_x 1
		.amdhsa_system_sgpr_workgroup_id_y 0
		.amdhsa_system_sgpr_workgroup_id_z 0
		.amdhsa_system_sgpr_workgroup_info 0
		.amdhsa_system_vgpr_workitem_id 0
		.amdhsa_next_free_vgpr 196
		.amdhsa_next_free_sgpr 37
		.amdhsa_accum_offset 196
		.amdhsa_reserve_vcc 1
		.amdhsa_float_round_mode_32 0
		.amdhsa_float_round_mode_16_64 0
		.amdhsa_float_denorm_mode_32 3
		.amdhsa_float_denorm_mode_16_64 3
		.amdhsa_dx10_clamp 1
		.amdhsa_ieee_mode 1
		.amdhsa_fp16_overflow 0
		.amdhsa_tg_split 0
		.amdhsa_exception_fp_ieee_invalid_op 0
		.amdhsa_exception_fp_denorm_src 0
		.amdhsa_exception_fp_ieee_div_zero 0
		.amdhsa_exception_fp_ieee_overflow 0
		.amdhsa_exception_fp_ieee_underflow 0
		.amdhsa_exception_fp_ieee_inexact 0
		.amdhsa_exception_int_div_zero 0
	.end_amdhsa_kernel

amdhsa.kernels:
  - .agpr_count:     0
    .args:
      - .actual_access:  read_only
        .address_space:  global
        .offset:         0
        .size:           8
        .value_kind:     global_buffer
      - .actual_access:  read_only
        .address_space:  global
        .offset:         8
        .size:           8
        .value_kind:     global_buffer
      - .actual_access:  read_only
        .address_space:  global
        .offset:         16
        .size:           8
        .value_kind:     global_buffer
      - .actual_access:  write_only
        .address_space:  global
        .offset:         24
        .size:           8
        .value_kind:     global_buffer
      - .actual_access:  write_only
        .address_space:  global
        .offset:         32
        .size:           8
        .value_kind:     global_buffer
    .group_segment_fixed_size: 0
    .kernarg_segment_align: 8
    .kernarg_segment_size: 40
    .language:       OpenCL C
    .language_version:
      - 2
      - 0
    .max_flat_workgroup_size: 256
    .name:           _Z12wprep_kernelPKfS0_S0_PDF16_Pj
    .private_segment_fixed_size: 0
    .sgpr_count:     18
    .sgpr_spill_count: 0
    .symbol:         _Z12wprep_kernelPKfS0_S0_PDF16_Pj.kd
    .uniform_work_group_size: 1
    .uses_dynamic_stack: false
    .vgpr_count:     12
    .vgpr_spill_count: 0
    .wavefront_size: 64
  - .agpr_count:     0
    .args:
      - .actual_access:  read_only
        .address_space:  global
        .offset:         0
        .size:           8
        .value_kind:     global_buffer
      - .actual_access:  read_only
        .address_space:  global
        .offset:         8
        .size:           8
        .value_kind:     global_buffer
      - .actual_access:  read_only
        .address_space:  global
        .offset:         16
        .size:           8
        .value_kind:     global_buffer
      - .actual_access:  read_only
        .address_space:  global
        .offset:         24
        .size:           8
        .value_kind:     global_buffer
      - .actual_access:  read_only
        .address_space:  global
        .offset:         32
        .size:           8
        .value_kind:     global_buffer
      - .actual_access:  read_only
        .address_space:  global
        .offset:         40
        .size:           8
        .value_kind:     global_buffer
      - .actual_access:  read_only
        .address_space:  global
        .offset:         48
        .size:           8
        .value_kind:     global_buffer
      - .actual_access:  write_only
        .address_space:  global
        .offset:         56
        .size:           8
        .value_kind:     global_buffer
      - .actual_access:  write_only
        .address_space:  global
        .offset:         64
        .size:           8
        .value_kind:     global_buffer
      - .actual_access:  write_only
        .address_space:  global
        .offset:         72
        .size:           8
        .value_kind:     global_buffer
      - .address_space:  global
        .offset:         80
        .size:           8
        .value_kind:     global_buffer
    .group_segment_fixed_size: 0
    .kernarg_segment_align: 8
    .kernarg_segment_size: 88
    .language:       OpenCL C
    .language_version:
      - 2
      - 0
    .max_flat_workgroup_size: 512
    .name:           _Z11proj_kernelPKfS0_S0_PKDF16_S0_S0_S0_PDF16_S3_S3_Pj
    .private_segment_fixed_size: 0
    .sgpr_count:     54
    .sgpr_spill_count: 0
    .symbol:         _Z11proj_kernelPKfS0_S0_PKDF16_S0_S0_S0_PDF16_S3_S3_Pj.kd
    .uniform_work_group_size: 1
    .uses_dynamic_stack: false
    .vgpr_count:     256
    .vgpr_spill_count: 0
    .wavefront_size: 64
  - .agpr_count:     0
    .args:
      - .actual_access:  read_only
        .address_space:  global
        .offset:         0
        .size:           8
        .value_kind:     global_buffer
      - .address_space:  global
        .offset:         8
        .size:           8
        .value_kind:     global_buffer
      - .address_space:  global
        .offset:         16
        .size:           8
        .value_kind:     global_buffer
      - .actual_access:  read_only
        .address_space:  global
        .offset:         24
        .size:           8
        .value_kind:     global_buffer
      - .actual_access:  write_only
        .address_space:  global
        .offset:         32
        .size:           8
        .value_kind:     global_buffer
    .group_segment_fixed_size: 0
    .kernarg_segment_align: 8
    .kernarg_segment_size: 40
    .language:       OpenCL C
    .language_version:
      - 2
      - 0
    .max_flat_workgroup_size: 512
    .name:           _Z11attn_kernelPKDF16_S0_S0_PKjPf
    .private_segment_fixed_size: 0
    .sgpr_count:     43
    .sgpr_spill_count: 0
    .symbol:         _Z11attn_kernelPKDF16_S0_S0_PKjPf.kd
    .uniform_work_group_size: 1
    .uses_dynamic_stack: false
    .vgpr_count:     196
    .vgpr_spill_count: 0
    .wavefront_size: 64
